# v19 + bar2 first-use census loads issued back-to-back instead of serialized
# speedup vs baseline: 1.0240x; 1.0035x over previous
; __device__ __forceinline__ unsigned xb_ld(unsigned* p)              { return __hip_atomic_load(p, __ATOMIC_RELAXED, __HIP_MEMORY_SCOPE_AGENT); }
; __device__ __forceinline__ void xcd_barrier_complete(unsigned* bar, unsigned x, unsigned& nloc, unsigned& nx, const unsigned G) {
;     unsigned sum, cnt, mine, sp = 0u;
;     for (;;) {
;         sum = 0u; cnt = 0u; mine = 0u;
; #pragma unroll
;         for (unsigned j = 0; j < 16; ++j) { const unsigned c = xb_ld(&bar[XB_XCNT(j)]); sum += c; cnt += (c > 0u) ? 1u : 0u; mine = (j == x) ? c : mine; }
;         if (sum == G) break;
;         __builtin_amdgcn_s_sleep(1);
;         if ((++sp & 255u) == 0u) { if (xb_ld(&bar[XB_TMO])) break; if (sp > XB_SPIN_CAP) { atomicAdd(&bar[XB_TMO], 1u); break; } }
;     }
;     nloc = mine > 0u ? mine : 1u; nx = cnt > 0u ? cnt : 1u;
; }
.LBB0_690:
	v_readlane_b32 s8, v251, 10
	v_readlane_b32 s9, v251, 11
	s_mov_b64 s[34:35], -1
	s_mov_b64 s[38:39], -1
	s_waitcnt lgkmcnt(0)
	s_nop 3
	global_load_dword v1, v195, s[8:9] sc1
	global_load_dword v2, v195, s[8:9] offset:256 sc1
	global_load_dword v3, v195, s[8:9] offset:512 sc1
	global_load_dword v4, v195, s[8:9] offset:768 sc1
	global_load_dword v5, v195, s[8:9] offset:1024 sc1
	global_load_dword v6, v195, s[8:9] offset:1280 sc1
	global_load_dword v7, v195, s[8:9] offset:1536 sc1
	global_load_dword v8, v195, s[8:9] offset:1792 sc1
	global_load_dword v9, v195, s[8:9] offset:2048 sc1
	global_load_dword v10, v195, s[8:9] offset:2304 sc1
	global_load_dword v11, v195, s[8:9] offset:2560 sc1
	global_load_dword v12, v195, s[8:9] offset:2816 sc1
	global_load_dword v13, v195, s[8:9] offset:3072 sc1
	global_load_dword v14, v195, s[8:9] offset:3328 sc1
	global_load_dword v15, v195, s[8:9] offset:3584 sc1
	global_load_dword v16, v195, s[8:9] offset:3840 sc1
	s_movk_i32 s8, 0xa0
	s_waitcnt vmcnt(0)
	v_add_u32_e32 v17, v2, v1
	v_add_u32_e32 v17, v17, v3
	v_add_u32_e32 v17, v17, v4
	v_add_u32_e32 v17, v17, v5
	v_add_u32_e32 v17, v17, v6
	v_add_u32_e32 v17, v17, v7
	v_add_u32_e32 v17, v17, v8
	v_add_u32_e32 v17, v17, v9
	v_add_u32_e32 v17, v17, v10
	v_add_u32_e32 v17, v17, v11
	v_add_u32_e32 v17, v17, v12
	v_add_u32_e32 v17, v17, v13
	v_add_u32_e32 v17, v17, v14
	v_add_u32_e32 v17, v17, v15
	v_add_u32_e32 v17, v17, v16
	v_cmp_eq_u32_e32 vcc, s8, v17
	s_cbranch_vccnz .LBB0_689
	s_and_b32 s8, s4, 0xff
	s_cmp_eq_u32 s8, 0
	s_mov_b64 s[40:41], -1
	s_sleep 1
	s_cbranch_scc1 .LBB0_694
	s_and_b64 vcc, exec, s[40:41]
	s_cbranch_vccz .LBB0_689
